# t10_ld_sc1nt
# speedup vs baseline: 1.0487x; 1.0244x over previous
_Z11align_fusedPKfS0_PKiPf:
	s_load_dwordx8 s[4:11], s[0:1], 0x0
	s_sub_u32 s2, 0x1fff, s2
	s_mul_i32 s12, s2, 0x5dc0
	v_and_b32_e32 v7, 63, v0
	v_readfirstlane_b32 s13, v0
	v_lshlrev_b32_e32 v1, 4, v7
	v_mul_u32_u24_e32 v3, 12, v7
	s_mul_i32 s18, s13, 96
	s_mul_i32 s3, s13, 6
	s_sub_u32 s3, 0x49c, s3
	v_cmp_gt_u32_e64 s[14:15], s3, v7
	v_add_u32_e32 v2, s18, v1
	v_add_u32_e32 v3, s18, v3
	v_add_u32_e32 v4, 0x600, v3
	s_add_u32 s12, s12, s18
	s_add_u32 s12, s12, 0x800
	s_waitcnt lgkmcnt(0)
	s_add_u32 s4, s4, s12
	s_addc_u32 s5, s5, 0
	s_add_u32 s10, s10, s12
	s_addc_u32 s11, s11, 0
	s_cmp_lg_u32 s13, 0
	s_cbranch_scc1 .Lbulk_waves
	v_lshlrev_b32_e32 v5, 2, v7
	global_load_dword v5, v5, s[8:9]
	global_load_dwordx3 v[44:46], v3, s[6:7] nt
	global_load_dwordx4 v[8:11], v1, s[4:5] offset:-2048 sc1 nt
	global_load_dwordx4 v[12:15], v1, s[4:5] offset:-1024 sc1 nt
	global_load_dwordx4 v[16:19], v1, s[4:5] offset:0 sc1 nt
	global_load_dwordx4 v[20:23], v1, s[4:5] offset:1024 sc1 nt
	global_load_dwordx4 v[24:27], v1, s[4:5] offset:2048 sc1 nt
	global_load_dwordx4 v[28:31], v1, s[4:5] offset:3072 sc1 nt
	s_mov_b32 s20, 0
	s_mov_b32 s21, 0x10000
	s_mov_b32 s22, 0
	s_mov_b32 s23, 0x20000
	s_mov_b32 s24, 0
	s_mov_b32 s25, 0x40000
	s_mov_b32 s26, 0
	s_mov_b32 s27, 0x80000
	s_waitcnt vmcnt(6)
	v_mul_u32_u24_e32 v5, 12, v5
	v_add_f32_dpp v52, v44, v44 quad_perm:[1,0,3,2] row_mask:0xf bank_mask:0xf
	v_add_f32_dpp v53, v45, v45 quad_perm:[1,0,3,2] row_mask:0xf bank_mask:0xf
	v_add_f32_dpp v54, v46, v46 quad_perm:[1,0,3,2] row_mask:0xf bank_mask:0xf
	v_add_f32_dpp v52, v52, v52 quad_perm:[2,3,0,1] row_mask:0xf bank_mask:0xf
	v_add_f32_dpp v53, v53, v53 quad_perm:[2,3,0,1] row_mask:0xf bank_mask:0xf
	v_add_f32_dpp v54, v54, v54 quad_perm:[2,3,0,1] row_mask:0xf bank_mask:0xf
	v_add_f32_dpp v52, v52, v52 row_half_mirror row_mask:0xf bank_mask:0xf
	v_add_f32_dpp v53, v53, v53 row_half_mirror row_mask:0xf bank_mask:0xf
	v_add_f32_dpp v54, v54, v54 row_half_mirror row_mask:0xf bank_mask:0xf
	v_add_f32_dpp v52, v52, v52 row_mirror row_mask:0xf bank_mask:0xf
	v_add_f32_dpp v53, v53, v53 row_mirror row_mask:0xf bank_mask:0xf
	v_add_f32_dpp v54, v54, v54 row_mirror row_mask:0xf bank_mask:0xf
	v_add_f32_dpp v52, v52, v52 row_bcast:15 row_mask:0xa bank_mask:0xf
	v_add_f32_dpp v53, v53, v53 row_bcast:15 row_mask:0xa bank_mask:0xf
	v_add_f32_dpp v54, v54, v54 row_bcast:15 row_mask:0xa bank_mask:0xf
	v_add_f32_dpp v52, v52, v52 row_bcast:31 row_mask:0xc bank_mask:0xf
	v_add_f32_dpp v53, v53, v53 row_bcast:31 row_mask:0xc bank_mask:0xf
	v_add_f32_dpp v54, v54, v54 row_bcast:31 row_mask:0xc bank_mask:0xf
	v_readlane_b32 s28, v52, 63
	v_readlane_b32 s29, v53, 63
	v_readlane_b32 s30, v54, 63
	v_mov_b32_e32 v52, s28
	v_mov_b32_e32 v53, s29
	v_mov_b32_e32 v54, s30
	v_fmac_f32_e32 v44, 0xbc800000, v52
	v_fmac_f32_e32 v45, 0xbc800000, v53
	v_fmac_f32_e32 v46, 0xbc800000, v54
	s_waitcnt vmcnt(0)
	ds_write_b128 v2, v[8:11]
	ds_write_b128 v2, v[12:15] offset:1024
	ds_write_b128 v2, v[16:19] offset:2048
	ds_write_b128 v2, v[20:23] offset:3072
	ds_write_b128 v2, v[24:27] offset:4096
	ds_write_b128 v2, v[28:31] offset:5120
	s_waitcnt lgkmcnt(0)
	s_barrier
	ds_read_b32 v48, v5
	ds_read_b32 v49, v5 offset:4
	ds_read_b32 v50, v5 offset:8
	s_waitcnt lgkmcnt(0)
	v_add_f32_dpp v52, v48, v48 quad_perm:[1,0,3,2] row_mask:0xf bank_mask:0xf
	v_add_f32_dpp v53, v49, v49 quad_perm:[1,0,3,2] row_mask:0xf bank_mask:0xf
	v_add_f32_dpp v54, v50, v50 quad_perm:[1,0,3,2] row_mask:0xf bank_mask:0xf
	v_add_f32_dpp v52, v52, v52 quad_perm:[2,3,0,1] row_mask:0xf bank_mask:0xf
	v_add_f32_dpp v53, v53, v53 quad_perm:[2,3,0,1] row_mask:0xf bank_mask:0xf
	v_add_f32_dpp v54, v54, v54 quad_perm:[2,3,0,1] row_mask:0xf bank_mask:0xf
	v_add_f32_dpp v52, v52, v52 row_half_mirror row_mask:0xf bank_mask:0xf
	v_add_f32_dpp v53, v53, v53 row_half_mirror row_mask:0xf bank_mask:0xf
	v_add_f32_dpp v54, v54, v54 row_half_mirror row_mask:0xf bank_mask:0xf
	v_add_f32_dpp v52, v52, v52 row_mirror row_mask:0xf bank_mask:0xf
	v_add_f32_dpp v53, v53, v53 row_mirror row_mask:0xf bank_mask:0xf
	v_add_f32_dpp v54, v54, v54 row_mirror row_mask:0xf bank_mask:0xf
	v_add_f32_dpp v52, v52, v52 row_bcast:15 row_mask:0xa bank_mask:0xf
	v_add_f32_dpp v53, v53, v53 row_bcast:15 row_mask:0xa bank_mask:0xf
	v_add_f32_dpp v54, v54, v54 row_bcast:15 row_mask:0xa bank_mask:0xf
	v_add_f32_dpp v52, v52, v52 row_bcast:31 row_mask:0xc bank_mask:0xf
	v_add_f32_dpp v53, v53, v53 row_bcast:31 row_mask:0xc bank_mask:0xf
	v_add_f32_dpp v54, v54, v54 row_bcast:31 row_mask:0xc bank_mask:0xf
	v_readlane_b32 s32, v52, 63
	v_readlane_b32 s33, v53, 63
	v_readlane_b32 s34, v54, 63
	v_mov_b32_e32 v52, s32
	v_mov_b32_e32 v53, s33
	v_mov_b32_e32 v54, s34
	v_fmac_f32_e32 v48, 0xbc800000, v52
	v_fmac_f32_e32 v49, 0xbc800000, v53
	v_fmac_f32_e32 v50, 0xbc800000, v54
	v_mul_f32_e32 v52, v48, v44
	v_mul_f32_e32 v53, v48, v45
	v_mul_f32_e32 v54, v48, v46
	v_mul_f32_e32 v55, v49, v44
	v_mul_f32_e32 v56, v49, v45
	v_mul_f32_e32 v57, v49, v46
	v_mul_f32_e32 v58, v50, v44
	v_mul_f32_e32 v59, v50, v45
	v_mul_f32_e32 v60, v50, v46
	v_add_f32_dpp v52, v52, v52 quad_perm:[1,0,3,2] row_mask:0xf bank_mask:0xf
	v_add_f32_dpp v53, v53, v53 quad_perm:[1,0,3,2] row_mask:0xf bank_mask:0xf
	v_add_f32_dpp v54, v54, v54 quad_perm:[1,0,3,2] row_mask:0xf bank_mask:0xf
	v_add_f32_dpp v55, v55, v55 quad_perm:[1,0,3,2] row_mask:0xf bank_mask:0xf
	v_add_f32_dpp v56, v56, v56 quad_perm:[1,0,3,2] row_mask:0xf bank_mask:0xf
	v_add_f32_dpp v57, v57, v57 quad_perm:[1,0,3,2] row_mask:0xf bank_mask:0xf
	v_add_f32_dpp v58, v58, v58 quad_perm:[1,0,3,2] row_mask:0xf bank_mask:0xf
	v_add_f32_dpp v59, v59, v59 quad_perm:[1,0,3,2] row_mask:0xf bank_mask:0xf
	v_add_f32_dpp v60, v60, v60 quad_perm:[1,0,3,2] row_mask:0xf bank_mask:0xf
	v_add_f32_dpp v52, v52, v52 quad_perm:[2,3,0,1] row_mask:0xf bank_mask:0xf
	v_add_f32_dpp v53, v53, v53 quad_perm:[2,3,0,1] row_mask:0xf bank_mask:0xf
	v_add_f32_dpp v54, v54, v54 quad_perm:[2,3,0,1] row_mask:0xf bank_mask:0xf
	v_add_f32_dpp v55, v55, v55 quad_perm:[2,3,0,1] row_mask:0xf bank_mask:0xf
	v_add_f32_dpp v56, v56, v56 quad_perm:[2,3,0,1] row_mask:0xf bank_mask:0xf
	v_add_f32_dpp v57, v57, v57 quad_perm:[2,3,0,1] row_mask:0xf bank_mask:0xf
	v_add_f32_dpp v58, v58, v58 quad_perm:[2,3,0,1] row_mask:0xf bank_mask:0xf
	v_add_f32_dpp v59, v59, v59 quad_perm:[2,3,0,1] row_mask:0xf bank_mask:0xf
	v_add_f32_dpp v60, v60, v60 quad_perm:[2,3,0,1] row_mask:0xf bank_mask:0xf
	v_add_f32_dpp v52, v52, v52 row_half_mirror row_mask:0xf bank_mask:0xf
	v_add_f32_dpp v53, v53, v53 row_half_mirror row_mask:0xf bank_mask:0xf
	v_add_f32_dpp v54, v54, v54 row_half_mirror row_mask:0xf bank_mask:0xf
	v_add_f32_dpp v55, v55, v55 row_half_mirror row_mask:0xf bank_mask:0xf
	v_add_f32_dpp v56, v56, v56 row_half_mirror row_mask:0xf bank_mask:0xf
	v_add_f32_dpp v57, v57, v57 row_half_mirror row_mask:0xf bank_mask:0xf
	v_add_f32_dpp v58, v58, v58 row_half_mirror row_mask:0xf bank_mask:0xf
	v_add_f32_dpp v59, v59, v59 row_half_mirror row_mask:0xf bank_mask:0xf
	v_add_f32_dpp v60, v60, v60 row_half_mirror row_mask:0xf bank_mask:0xf
	v_add_f32_dpp v52, v52, v52 row_mirror row_mask:0xf bank_mask:0xf
	v_add_f32_dpp v53, v53, v53 row_mirror row_mask:0xf bank_mask:0xf
	v_add_f32_dpp v54, v54, v54 row_mirror row_mask:0xf bank_mask:0xf
	v_add_f32_dpp v55, v55, v55 row_mirror row_mask:0xf bank_mask:0xf
	v_add_f32_dpp v56, v56, v56 row_mirror row_mask:0xf bank_mask:0xf
	v_add_f32_dpp v57, v57, v57 row_mirror row_mask:0xf bank_mask:0xf
	v_add_f32_dpp v58, v58, v58 row_mirror row_mask:0xf bank_mask:0xf
	v_add_f32_dpp v59, v59, v59 row_mirror row_mask:0xf bank_mask:0xf
	v_add_f32_dpp v60, v60, v60 row_mirror row_mask:0xf bank_mask:0xf
	v_add_f32_dpp v52, v52, v52 row_bcast:15 row_mask:0xa bank_mask:0xf
	v_add_f32_dpp v53, v53, v53 row_bcast:15 row_mask:0xa bank_mask:0xf
	v_add_f32_dpp v54, v54, v54 row_bcast:15 row_mask:0xa bank_mask:0xf
	v_add_f32_dpp v55, v55, v55 row_bcast:15 row_mask:0xa bank_mask:0xf
	v_add_f32_dpp v56, v56, v56 row_bcast:15 row_mask:0xa bank_mask:0xf
	v_add_f32_dpp v57, v57, v57 row_bcast:15 row_mask:0xa bank_mask:0xf
	v_add_f32_dpp v58, v58, v58 row_bcast:15 row_mask:0xa bank_mask:0xf
	v_add_f32_dpp v59, v59, v59 row_bcast:15 row_mask:0xa bank_mask:0xf
	v_add_f32_dpp v60, v60, v60 row_bcast:15 row_mask:0xa bank_mask:0xf
	v_add_f32_dpp v52, v52, v52 row_bcast:31 row_mask:0xc bank_mask:0xf
	v_add_f32_dpp v53, v53, v53 row_bcast:31 row_mask:0xc bank_mask:0xf
	v_add_f32_dpp v54, v54, v54 row_bcast:31 row_mask:0xc bank_mask:0xf
	v_add_f32_dpp v55, v55, v55 row_bcast:31 row_mask:0xc bank_mask:0xf
	v_add_f32_dpp v56, v56, v56 row_bcast:31 row_mask:0xc bank_mask:0xf
	v_add_f32_dpp v57, v57, v57 row_bcast:31 row_mask:0xc bank_mask:0xf
	v_add_f32_dpp v58, v58, v58 row_bcast:31 row_mask:0xc bank_mask:0xf
	v_add_f32_dpp v59, v59, v59 row_bcast:31 row_mask:0xc bank_mask:0xf
	v_add_f32_dpp v60, v60, v60 row_bcast:31 row_mask:0xc bank_mask:0xf
	v_cndmask_b32_e64 v52, v52, v55, s[22:23]
	v_cndmask_b32_e64 v53, v53, v56, s[22:23]
	v_cndmask_b32_e64 v54, v54, v57, s[22:23]
	v_cndmask_b32_e64 v52, v52, v58, s[24:25]
	v_cndmask_b32_e64 v53, v53, v59, s[24:25]
	v_cndmask_b32_e64 v54, v54, v60, s[24:25]
	v_cndmask_b32_e64 v52, v52, 0, s[26:27]
	v_cndmask_b32_e64 v53, v53, 0, s[26:27]
	v_cndmask_b32_e64 v54, v54, 0, s[26:27]
	v_cndmask_b32_e64 v40, 0, 1.0, s[20:21]
	v_cndmask_b32_e64 v41, 0, 1.0, s[22:23]
	v_cndmask_b32_e64 v42, 0, 1.0, s[24:25]
	v_mul_f32_e32 v55, v52, v52
	v_mul_f32_e32 v56, v53, v53
	v_mul_f32_e32 v57, v52, v53
	v_add_f32_dpp v55, v55, v55 quad_perm:[1,0,3,2] row_mask:0xf bank_mask:0xf
	v_add_f32_dpp v56, v56, v56 quad_perm:[1,0,3,2] row_mask:0xf bank_mask:0xf
	v_add_f32_dpp v57, v57, v57 quad_perm:[1,0,3,2] row_mask:0xf bank_mask:0xf
	v_add_f32_dpp v55, v55, v55 quad_perm:[2,3,0,1] row_mask:0xf bank_mask:0xf
	v_add_f32_dpp v56, v56, v56 quad_perm:[2,3,0,1] row_mask:0xf bank_mask:0xf
	v_add_f32_dpp v57, v57, v57 quad_perm:[2,3,0,1] row_mask:0xf bank_mask:0xf
	v_sub_f32_e32 v60, v56, v55
	v_mul_f32_e32 v58, v57, v57
	v_cmp_gt_f32_e32 vcc, 0, v60
	v_mul_f32_e32 v59, v60, v60
	v_fmac_f32_e32 v59, 4.0, v58
	v_sqrt_f32_e32 v59, v59
	s_nop 0
	v_add_f32_e64 v59, |v60|, v59
	v_add_f32_e32 v59, 0x0da24260, v59
	v_rcp_f32_e32 v59, v59
	v_add_f32_e32 v58, v57, v57
	v_mul_f32_e32 v59, v58, v59
	v_cndmask_b32_e64 v59, v59, -v59, vcc
	v_fma_f32 v58, v59, v59, 1.0
	v_rsq_f32_e32 v61, v58
	s_nop 0
	v_mul_f32_e32 v62, v61, v59
	v_mul_f32_e32 v55, v62, v53
	v_mul_f32_e32 v56, v62, v52
	v_fma_f32 v52, v61, v52, -v55
	v_fma_f32 v53, v61, v53, v56
	v_mul_f32_e32 v55, v52, v52
	v_mul_f32_e32 v56, v54, v54
	v_mul_f32_e32 v57, v52, v54
	v_add_f32_dpp v55, v55, v55 quad_perm:[1,0,3,2] row_mask:0xf bank_mask:0xf
	v_add_f32_dpp v56, v56, v56 quad_perm:[1,0,3,2] row_mask:0xf bank_mask:0xf
	v_add_f32_dpp v57, v57, v57 quad_perm:[1,0,3,2] row_mask:0xf bank_mask:0xf
	v_add_f32_dpp v55, v55, v55 quad_perm:[2,3,0,1] row_mask:0xf bank_mask:0xf
	v_add_f32_dpp v56, v56, v56 quad_perm:[2,3,0,1] row_mask:0xf bank_mask:0xf
	v_add_f32_dpp v57, v57, v57 quad_perm:[2,3,0,1] row_mask:0xf bank_mask:0xf
	v_sub_f32_e32 v60, v56, v55
	v_mul_f32_e32 v58, v57, v57
	v_cmp_gt_f32_e32 vcc, 0, v60
	v_mul_f32_e32 v59, v60, v60
	v_fmac_f32_e32 v59, 4.0, v58
	v_sqrt_f32_e32 v59, v59
	v_mul_f32_e32 v63, v62, v41
	v_mul_f32_e32 v43, v62, v40
	v_fma_f32 v40, v61, v40, -v63
	v_fma_f32 v41, v61, v41, v43
	v_add_f32_e64 v59, |v60|, v59
	v_add_f32_e32 v59, 0x0da24260, v59
	v_rcp_f32_e32 v59, v59
	v_add_f32_e32 v58, v57, v57
	v_mul_f32_e32 v59, v58, v59
	v_cndmask_b32_e64 v59, v59, -v59, vcc
	v_fma_f32 v58, v59, v59, 1.0
	v_rsq_f32_e32 v61, v58
	s_nop 0
	v_mul_f32_e32 v62, v61, v59
	v_mul_f32_e32 v55, v62, v54
	v_mul_f32_e32 v56, v62, v52
	v_fma_f32 v52, v61, v52, -v55
	v_fma_f32 v54, v61, v54, v56
	v_mul_f32_e32 v55, v53, v53
	v_mul_f32_e32 v56, v54, v54
	v_mul_f32_e32 v57, v53, v54
	v_add_f32_dpp v55, v55, v55 quad_perm:[1,0,3,2] row_mask:0xf bank_mask:0xf
	v_add_f32_dpp v56, v56, v56 quad_perm:[1,0,3,2] row_mask:0xf bank_mask:0xf
	v_add_f32_dpp v57, v57, v57 quad_perm:[1,0,3,2] row_mask:0xf bank_mask:0xf
	v_add_f32_dpp v55, v55, v55 quad_perm:[2,3,0,1] row_mask:0xf bank_mask:0xf
	v_add_f32_dpp v56, v56, v56 quad_perm:[2,3,0,1] row_mask:0xf bank_mask:0xf
	v_add_f32_dpp v57, v57, v57 quad_perm:[2,3,0,1] row_mask:0xf bank_mask:0xf
	v_sub_f32_e32 v60, v56, v55
	v_mul_f32_e32 v58, v57, v57
	v_cmp_gt_f32_e32 vcc, 0, v60
	v_mul_f32_e32 v59, v60, v60
	v_fmac_f32_e32 v59, 4.0, v58
	v_sqrt_f32_e32 v59, v59
	v_mul_f32_e32 v63, v62, v42
	v_mul_f32_e32 v43, v62, v40
	v_fma_f32 v40, v61, v40, -v63
	v_fma_f32 v42, v61, v42, v43
	v_add_f32_e64 v59, |v60|, v59
	v_add_f32_e32 v59, 0x0da24260, v59
	v_rcp_f32_e32 v59, v59
	v_add_f32_e32 v58, v57, v57
	v_mul_f32_e32 v59, v58, v59
	v_cndmask_b32_e64 v59, v59, -v59, vcc
	v_fma_f32 v58, v59, v59, 1.0
	v_rsq_f32_e32 v61, v58
	s_nop 0
	v_mul_f32_e32 v62, v61, v59
	v_mul_f32_e32 v55, v62, v54
	v_mul_f32_e32 v56, v62, v53
	v_fma_f32 v53, v61, v53, -v55
	v_fma_f32 v54, v61, v54, v56
	v_mul_f32_e32 v55, v52, v52
	v_mul_f32_e32 v56, v53, v53
	v_mul_f32_e32 v57, v52, v53
	v_add_f32_dpp v55, v55, v55 quad_perm:[1,0,3,2] row_mask:0xf bank_mask:0xf
	v_add_f32_dpp v56, v56, v56 quad_perm:[1,0,3,2] row_mask:0xf bank_mask:0xf
	v_add_f32_dpp v57, v57, v57 quad_perm:[1,0,3,2] row_mask:0xf bank_mask:0xf
	v_add_f32_dpp v55, v55, v55 quad_perm:[2,3,0,1] row_mask:0xf bank_mask:0xf
	v_add_f32_dpp v56, v56, v56 quad_perm:[2,3,0,1] row_mask:0xf bank_mask:0xf
	v_add_f32_dpp v57, v57, v57 quad_perm:[2,3,0,1] row_mask:0xf bank_mask:0xf
	v_sub_f32_e32 v60, v56, v55
	v_mul_f32_e32 v58, v57, v57
	v_cmp_gt_f32_e32 vcc, 0, v60
	v_mul_f32_e32 v59, v60, v60
	v_fmac_f32_e32 v59, 4.0, v58
	v_sqrt_f32_e32 v59, v59
	v_mul_f32_e32 v63, v62, v42
	v_mul_f32_e32 v43, v62, v41
	v_fma_f32 v41, v61, v41, -v63
	v_fma_f32 v42, v61, v42, v43
	v_add_f32_e64 v59, |v60|, v59
	v_add_f32_e32 v59, 0x0da24260, v59
	v_rcp_f32_e32 v59, v59
	v_add_f32_e32 v58, v57, v57
	v_mul_f32_e32 v59, v58, v59
	v_cndmask_b32_e64 v59, v59, -v59, vcc
	v_fma_f32 v58, v59, v59, 1.0
	v_rsq_f32_e32 v61, v58
	s_nop 0
	v_mul_f32_e32 v62, v61, v59
	v_mul_f32_e32 v55, v62, v53
	v_mul_f32_e32 v56, v62, v52
	v_fma_f32 v52, v61, v52, -v55
	v_fma_f32 v53, v61, v53, v56
	v_mul_f32_e32 v55, v52, v52
	v_mul_f32_e32 v56, v54, v54
	v_mul_f32_e32 v57, v52, v54
	v_add_f32_dpp v55, v55, v55 quad_perm:[1,0,3,2] row_mask:0xf bank_mask:0xf
	v_add_f32_dpp v56, v56, v56 quad_perm:[1,0,3,2] row_mask:0xf bank_mask:0xf
	v_add_f32_dpp v57, v57, v57 quad_perm:[1,0,3,2] row_mask:0xf bank_mask:0xf
	v_add_f32_dpp v55, v55, v55 quad_perm:[2,3,0,1] row_mask:0xf bank_mask:0xf
	v_add_f32_dpp v56, v56, v56 quad_perm:[2,3,0,1] row_mask:0xf bank_mask:0xf
	v_add_f32_dpp v57, v57, v57 quad_perm:[2,3,0,1] row_mask:0xf bank_mask:0xf
	v_sub_f32_e32 v60, v56, v55
	v_mul_f32_e32 v58, v57, v57
	v_cmp_gt_f32_e32 vcc, 0, v60
	v_mul_f32_e32 v59, v60, v60
	v_fmac_f32_e32 v59, 4.0, v58
	v_sqrt_f32_e32 v59, v59
	v_mul_f32_e32 v63, v62, v41
	v_mul_f32_e32 v43, v62, v40
	v_fma_f32 v40, v61, v40, -v63
	v_fma_f32 v41, v61, v41, v43
	v_add_f32_e64 v59, |v60|, v59
	v_add_f32_e32 v59, 0x0da24260, v59
	v_rcp_f32_e32 v59, v59
	v_add_f32_e32 v58, v57, v57
	v_mul_f32_e32 v59, v58, v59
	v_cndmask_b32_e64 v59, v59, -v59, vcc
	v_fma_f32 v58, v59, v59, 1.0
	v_rsq_f32_e32 v61, v58
	s_nop 0
	v_mul_f32_e32 v62, v61, v59
	v_mul_f32_e32 v55, v62, v54
	v_mul_f32_e32 v56, v62, v52
	v_fma_f32 v52, v61, v52, -v55
	v_fma_f32 v54, v61, v54, v56
	v_mul_f32_e32 v55, v53, v53
	v_mul_f32_e32 v56, v54, v54
	v_mul_f32_e32 v57, v53, v54
	v_add_f32_dpp v55, v55, v55 quad_perm:[1,0,3,2] row_mask:0xf bank_mask:0xf
	v_add_f32_dpp v56, v56, v56 quad_perm:[1,0,3,2] row_mask:0xf bank_mask:0xf
	v_add_f32_dpp v57, v57, v57 quad_perm:[1,0,3,2] row_mask:0xf bank_mask:0xf
	v_add_f32_dpp v55, v55, v55 quad_perm:[2,3,0,1] row_mask:0xf bank_mask:0xf
	v_add_f32_dpp v56, v56, v56 quad_perm:[2,3,0,1] row_mask:0xf bank_mask:0xf
	v_add_f32_dpp v57, v57, v57 quad_perm:[2,3,0,1] row_mask:0xf bank_mask:0xf
	v_sub_f32_e32 v60, v56, v55
	v_mul_f32_e32 v58, v57, v57
	v_cmp_gt_f32_e32 vcc, 0, v60
	v_mul_f32_e32 v59, v60, v60
	v_fmac_f32_e32 v59, 4.0, v58
	v_sqrt_f32_e32 v59, v59
	v_mul_f32_e32 v63, v62, v42
	v_mul_f32_e32 v43, v62, v40
	v_fma_f32 v40, v61, v40, -v63
	v_fma_f32 v42, v61, v42, v43
	v_add_f32_e64 v59, |v60|, v59
	v_add_f32_e32 v59, 0x0da24260, v59
	v_rcp_f32_e32 v59, v59
	v_add_f32_e32 v58, v57, v57
	v_mul_f32_e32 v59, v58, v59
	v_cndmask_b32_e64 v59, v59, -v59, vcc
	v_fma_f32 v58, v59, v59, 1.0
	v_rsq_f32_e32 v61, v58
	s_nop 0
	v_mul_f32_e32 v62, v61, v59
	v_mul_f32_e32 v55, v62, v54
	v_mul_f32_e32 v56, v62, v53
	v_fma_f32 v53, v61, v53, -v55
	v_fma_f32 v54, v61, v54, v56
	v_mul_f32_e32 v55, v52, v52
	v_mul_f32_e32 v56, v53, v53
	v_mul_f32_e32 v57, v52, v53
	v_add_f32_dpp v55, v55, v55 quad_perm:[1,0,3,2] row_mask:0xf bank_mask:0xf
	v_add_f32_dpp v56, v56, v56 quad_perm:[1,0,3,2] row_mask:0xf bank_mask:0xf
	v_add_f32_dpp v57, v57, v57 quad_perm:[1,0,3,2] row_mask:0xf bank_mask:0xf
	v_add_f32_dpp v55, v55, v55 quad_perm:[2,3,0,1] row_mask:0xf bank_mask:0xf
	v_add_f32_dpp v56, v56, v56 quad_perm:[2,3,0,1] row_mask:0xf bank_mask:0xf
	v_add_f32_dpp v57, v57, v57 quad_perm:[2,3,0,1] row_mask:0xf bank_mask:0xf
	v_sub_f32_e32 v60, v56, v55
	v_mul_f32_e32 v58, v57, v57
	v_cmp_gt_f32_e32 vcc, 0, v60
	v_mul_f32_e32 v59, v60, v60
	v_fmac_f32_e32 v59, 4.0, v58
	v_sqrt_f32_e32 v59, v59
	v_mul_f32_e32 v63, v62, v42
	v_mul_f32_e32 v43, v62, v41
	v_fma_f32 v41, v61, v41, -v63
	v_fma_f32 v42, v61, v42, v43
	v_add_f32_e64 v59, |v60|, v59
	v_add_f32_e32 v59, 0x0da24260, v59
	v_rcp_f32_e32 v59, v59
	v_add_f32_e32 v58, v57, v57
	v_mul_f32_e32 v59, v58, v59
	v_cndmask_b32_e64 v59, v59, -v59, vcc
	v_fma_f32 v58, v59, v59, 1.0
	v_rsq_f32_e32 v61, v58
	s_nop 0
	v_mul_f32_e32 v62, v61, v59
	v_mul_f32_e32 v55, v62, v53
	v_mul_f32_e32 v56, v62, v52
	v_fma_f32 v52, v61, v52, -v55
	v_fma_f32 v53, v61, v53, v56
	v_mul_f32_e32 v55, v52, v52
	v_mul_f32_e32 v56, v54, v54
	v_mul_f32_e32 v57, v52, v54
	v_add_f32_dpp v55, v55, v55 quad_perm:[1,0,3,2] row_mask:0xf bank_mask:0xf
	v_add_f32_dpp v56, v56, v56 quad_perm:[1,0,3,2] row_mask:0xf bank_mask:0xf
	v_add_f32_dpp v57, v57, v57 quad_perm:[1,0,3,2] row_mask:0xf bank_mask:0xf
	v_add_f32_dpp v55, v55, v55 quad_perm:[2,3,0,1] row_mask:0xf bank_mask:0xf
	v_add_f32_dpp v56, v56, v56 quad_perm:[2,3,0,1] row_mask:0xf bank_mask:0xf
	v_add_f32_dpp v57, v57, v57 quad_perm:[2,3,0,1] row_mask:0xf bank_mask:0xf
	v_sub_f32_e32 v60, v56, v55
	v_mul_f32_e32 v58, v57, v57
	v_cmp_gt_f32_e32 vcc, 0, v60
	v_mul_f32_e32 v59, v60, v60
	v_fmac_f32_e32 v59, 4.0, v58
	v_sqrt_f32_e32 v59, v59
	v_mul_f32_e32 v63, v62, v41
	v_mul_f32_e32 v43, v62, v40
	v_fma_f32 v40, v61, v40, -v63
	v_fma_f32 v41, v61, v41, v43
	v_add_f32_e64 v59, |v60|, v59
	v_add_f32_e32 v59, 0x0da24260, v59
	v_rcp_f32_e32 v59, v59
	v_add_f32_e32 v58, v57, v57
	v_mul_f32_e32 v59, v58, v59
	v_cndmask_b32_e64 v59, v59, -v59, vcc
	v_fma_f32 v58, v59, v59, 1.0
	v_rsq_f32_e32 v61, v58
	s_nop 0
	v_mul_f32_e32 v62, v61, v59
	v_mul_f32_e32 v55, v62, v54
	v_mul_f32_e32 v56, v62, v52
	v_fma_f32 v52, v61, v52, -v55
	v_fma_f32 v54, v61, v54, v56
	v_mul_f32_e32 v55, v53, v53
	v_mul_f32_e32 v56, v54, v54
	v_mul_f32_e32 v57, v53, v54
	v_add_f32_dpp v55, v55, v55 quad_perm:[1,0,3,2] row_mask:0xf bank_mask:0xf
	v_add_f32_dpp v56, v56, v56 quad_perm:[1,0,3,2] row_mask:0xf bank_mask:0xf
	v_add_f32_dpp v57, v57, v57 quad_perm:[1,0,3,2] row_mask:0xf bank_mask:0xf
	v_add_f32_dpp v55, v55, v55 quad_perm:[2,3,0,1] row_mask:0xf bank_mask:0xf
	v_add_f32_dpp v56, v56, v56 quad_perm:[2,3,0,1] row_mask:0xf bank_mask:0xf
	v_add_f32_dpp v57, v57, v57 quad_perm:[2,3,0,1] row_mask:0xf bank_mask:0xf
	v_sub_f32_e32 v60, v56, v55
	v_mul_f32_e32 v58, v57, v57
	v_cmp_gt_f32_e32 vcc, 0, v60
	v_mul_f32_e32 v59, v60, v60
	v_fmac_f32_e32 v59, 4.0, v58
	v_sqrt_f32_e32 v59, v59
	v_mul_f32_e32 v63, v62, v42
	v_mul_f32_e32 v43, v62, v40
	v_fma_f32 v40, v61, v40, -v63
	v_fma_f32 v42, v61, v42, v43
	v_add_f32_e64 v59, |v60|, v59
	v_add_f32_e32 v59, 0x0da24260, v59
	v_rcp_f32_e32 v59, v59
	v_add_f32_e32 v58, v57, v57
	v_mul_f32_e32 v59, v58, v59
	v_cndmask_b32_e64 v59, v59, -v59, vcc
	v_fma_f32 v58, v59, v59, 1.0
	v_rsq_f32_e32 v61, v58
	s_nop 0
	v_mul_f32_e32 v62, v61, v59
	v_mul_f32_e32 v55, v62, v54
	v_mul_f32_e32 v56, v62, v53
	v_fma_f32 v53, v61, v53, -v55
	v_fma_f32 v54, v61, v54, v56
	v_mul_f32_e32 v55, v52, v52
	v_mul_f32_e32 v56, v53, v53
	v_mul_f32_e32 v57, v52, v53
	v_add_f32_dpp v55, v55, v55 quad_perm:[1,0,3,2] row_mask:0xf bank_mask:0xf
	v_add_f32_dpp v56, v56, v56 quad_perm:[1,0,3,2] row_mask:0xf bank_mask:0xf
	v_add_f32_dpp v57, v57, v57 quad_perm:[1,0,3,2] row_mask:0xf bank_mask:0xf
	v_add_f32_dpp v55, v55, v55 quad_perm:[2,3,0,1] row_mask:0xf bank_mask:0xf
	v_add_f32_dpp v56, v56, v56 quad_perm:[2,3,0,1] row_mask:0xf bank_mask:0xf
	v_add_f32_dpp v57, v57, v57 quad_perm:[2,3,0,1] row_mask:0xf bank_mask:0xf
	v_sub_f32_e32 v60, v56, v55
	v_mul_f32_e32 v58, v57, v57
	v_cmp_gt_f32_e32 vcc, 0, v60
	v_mul_f32_e32 v59, v60, v60
	v_fmac_f32_e32 v59, 4.0, v58
	v_sqrt_f32_e32 v59, v59
	v_mul_f32_e32 v63, v62, v42
	v_mul_f32_e32 v43, v62, v41
	v_fma_f32 v41, v61, v41, -v63
	v_fma_f32 v42, v61, v42, v43
	v_add_f32_e64 v59, |v60|, v59
	v_add_f32_e32 v59, 0x0da24260, v59
	v_rcp_f32_e32 v59, v59
	v_add_f32_e32 v58, v57, v57
	v_mul_f32_e32 v59, v58, v59
	v_cndmask_b32_e64 v59, v59, -v59, vcc
	v_fma_f32 v58, v59, v59, 1.0
	v_rsq_f32_e32 v61, v58
	s_nop 0
	v_mul_f32_e32 v62, v61, v59
	v_mul_f32_e32 v55, v62, v53
	v_mul_f32_e32 v56, v62, v52
	v_fma_f32 v52, v61, v52, -v55
	v_fma_f32 v53, v61, v53, v56
	v_mul_f32_e32 v55, v52, v52
	v_mul_f32_e32 v56, v54, v54
	v_mul_f32_e32 v57, v52, v54
	v_add_f32_dpp v55, v55, v55 quad_perm:[1,0,3,2] row_mask:0xf bank_mask:0xf
	v_add_f32_dpp v56, v56, v56 quad_perm:[1,0,3,2] row_mask:0xf bank_mask:0xf
	v_add_f32_dpp v57, v57, v57 quad_perm:[1,0,3,2] row_mask:0xf bank_mask:0xf
	v_add_f32_dpp v55, v55, v55 quad_perm:[2,3,0,1] row_mask:0xf bank_mask:0xf
	v_add_f32_dpp v56, v56, v56 quad_perm:[2,3,0,1] row_mask:0xf bank_mask:0xf
	v_add_f32_dpp v57, v57, v57 quad_perm:[2,3,0,1] row_mask:0xf bank_mask:0xf
	v_sub_f32_e32 v60, v56, v55
	v_mul_f32_e32 v58, v57, v57
	v_cmp_gt_f32_e32 vcc, 0, v60
	v_mul_f32_e32 v59, v60, v60
	v_fmac_f32_e32 v59, 4.0, v58
	v_sqrt_f32_e32 v59, v59
	v_mul_f32_e32 v63, v62, v41
	v_mul_f32_e32 v43, v62, v40
	v_fma_f32 v40, v61, v40, -v63
	v_fma_f32 v41, v61, v41, v43
	v_add_f32_e64 v59, |v60|, v59
	v_add_f32_e32 v59, 0x0da24260, v59
	v_rcp_f32_e32 v59, v59
	v_add_f32_e32 v58, v57, v57
	v_mul_f32_e32 v59, v58, v59
	v_cndmask_b32_e64 v59, v59, -v59, vcc
	v_fma_f32 v58, v59, v59, 1.0
	v_rsq_f32_e32 v61, v58
	s_nop 0
	v_mul_f32_e32 v62, v61, v59
	v_mul_f32_e32 v55, v62, v54
	v_mul_f32_e32 v56, v62, v52
	v_fma_f32 v52, v61, v52, -v55
	v_fma_f32 v54, v61, v54, v56
	v_mul_f32_e32 v55, v53, v53
	v_mul_f32_e32 v56, v54, v54
	v_mul_f32_e32 v57, v53, v54
	v_add_f32_dpp v55, v55, v55 quad_perm:[1,0,3,2] row_mask:0xf bank_mask:0xf
	v_add_f32_dpp v56, v56, v56 quad_perm:[1,0,3,2] row_mask:0xf bank_mask:0xf
	v_add_f32_dpp v57, v57, v57 quad_perm:[1,0,3,2] row_mask:0xf bank_mask:0xf
	v_add_f32_dpp v55, v55, v55 quad_perm:[2,3,0,1] row_mask:0xf bank_mask:0xf
	v_add_f32_dpp v56, v56, v56 quad_perm:[2,3,0,1] row_mask:0xf bank_mask:0xf
	v_add_f32_dpp v57, v57, v57 quad_perm:[2,3,0,1] row_mask:0xf bank_mask:0xf
	v_sub_f32_e32 v60, v56, v55
	v_mul_f32_e32 v58, v57, v57
	v_cmp_gt_f32_e32 vcc, 0, v60
	v_mul_f32_e32 v59, v60, v60
	v_fmac_f32_e32 v59, 4.0, v58
	v_sqrt_f32_e32 v59, v59
	v_mul_f32_e32 v63, v62, v42
	v_mul_f32_e32 v43, v62, v40
	v_fma_f32 v40, v61, v40, -v63
	v_fma_f32 v42, v61, v42, v43
	v_add_f32_e64 v59, |v60|, v59
	v_add_f32_e32 v59, 0x0da24260, v59
	v_rcp_f32_e32 v59, v59
	v_add_f32_e32 v58, v57, v57
	v_mul_f32_e32 v59, v58, v59
	v_cndmask_b32_e64 v59, v59, -v59, vcc
	v_fma_f32 v58, v59, v59, 1.0
	v_rsq_f32_e32 v61, v58
	s_nop 0
	v_mul_f32_e32 v62, v61, v59
	v_mul_f32_e32 v55, v62, v54
	v_mul_f32_e32 v56, v62, v53
	v_fma_f32 v53, v61, v53, -v55
	v_fma_f32 v54, v61, v54, v56
	v_mul_f32_e32 v63, v62, v42
	v_mul_f32_e32 v43, v62, v41
	v_fma_f32 v41, v61, v41, -v63
	v_fma_f32 v42, v61, v42, v43
	v_mul_f32_e32 v55, v52, v52
	v_mul_f32_e32 v56, v53, v53
	v_mul_f32_e32 v57, v54, v54
	v_add_f32_dpp v55, v55, v55 quad_perm:[1,0,3,2] row_mask:0xf bank_mask:0xf
	v_add_f32_dpp v56, v56, v56 quad_perm:[1,0,3,2] row_mask:0xf bank_mask:0xf
	v_add_f32_dpp v57, v57, v57 quad_perm:[1,0,3,2] row_mask:0xf bank_mask:0xf
	v_add_f32_dpp v55, v55, v55 quad_perm:[2,3,0,1] row_mask:0xf bank_mask:0xf
	v_add_f32_dpp v56, v56, v56 quad_perm:[2,3,0,1] row_mask:0xf bank_mask:0xf
	v_add_f32_dpp v57, v57, v57 quad_perm:[2,3,0,1] row_mask:0xf bank_mask:0xf
	v_cmp_le_f32_e64 s[28:29], v55, v56
	v_cmp_le_f32_e64 s[30:31], v55, v57
	v_cmp_lt_f32_e32 vcc, v57, v56
	s_and_b64 s[28:29], s[28:29], s[30:31]
	s_andn2_b64 s[30:31], vcc, s[28:29]
	v_cndmask_b32_e64 v44, v52, v53, s[28:29]
	v_cndmask_b32_e64 v45, v54, v53, s[30:31]
	v_cndmask_b32_e64 v46, v40, v41, s[28:29]
	v_cndmask_b32_e64 v47, v42, v41, s[30:31]
	v_mul_f32_e32 v58, v44, v44
	s_nop 1
	v_add_f32_dpp v58, v58, v58 quad_perm:[1,0,3,2] row_mask:0xf bank_mask:0xf
	s_nop 1
	v_add_f32_dpp v58, v58, v58 quad_perm:[2,3,0,1] row_mask:0xf bank_mask:0xf
	v_max_f32_e32 v58, 0x3aa2425, v58
	v_rsq_f32_e32 v58, v58
	s_nop 0
	v_mul_f32_e32 v48, v44, v58
	v_mul_f32_e32 v59, v48, v45
	s_nop 1
	v_add_f32_dpp v59, v59, v59 quad_perm:[1,0,3,2] row_mask:0xf bank_mask:0xf
	s_nop 1
	v_add_f32_dpp v59, v59, v59 quad_perm:[2,3,0,1] row_mask:0xf bank_mask:0xf
	v_fma_f32 v49, -v59, v48, v45
	v_mul_f32_e32 v58, v49, v49
	s_nop 1
	v_add_f32_dpp v58, v58, v58 quad_perm:[1,0,3,2] row_mask:0xf bank_mask:0xf
	s_nop 1
	v_add_f32_dpp v58, v58, v58 quad_perm:[2,3,0,1] row_mask:0xf bank_mask:0xf
	v_max_f32_e32 v58, 0x3aa2425, v58
	v_rsq_f32_e32 v58, v58
	s_nop 0
	v_mul_f32_e32 v50, v49, v58
	v_mov_b32_dpp v43, v47 quad_perm:[2,0,1,3] row_mask:0xf bank_mask:0xf
	v_mov_b32_dpp v63, v47 quad_perm:[1,2,0,3] row_mask:0xf bank_mask:0xf
	v_mov_b32_dpp v62, v50 quad_perm:[2,0,1,3] row_mask:0xf bank_mask:0xf
	v_mov_b32_dpp v61, v50 quad_perm:[1,2,0,3] row_mask:0xf bank_mask:0xf
	v_mul_f32_dpp v60, v46, v43 quad_perm:[1,2,0,3] row_mask:0xf bank_mask:0xf
	v_mul_f32_dpp v51, v48, v62 quad_perm:[1,2,0,3] row_mask:0xf bank_mask:0xf
	s_nop 0
	v_fmac_f32_dpp v60, -v46, v63 quad_perm:[2,0,1,3] row_mask:0xf bank_mask:0xf
	v_fmac_f32_dpp v51, -v48, v61 quad_perm:[2,0,1,3] row_mask:0xf bank_mask:0xf
	v_mul_f32_dpp v52, v46, v48 quad_perm:[0,0,0,0] row_mask:0xf bank_mask:0xf
	v_mul_f32_dpp v53, v46, v48 quad_perm:[1,1,1,1] row_mask:0xf bank_mask:0xf
	v_mul_f32_dpp v54, v46, v48 quad_perm:[2,2,2,2] row_mask:0xf bank_mask:0xf
	v_fmac_f32_dpp v52, v47, v50 quad_perm:[0,0,0,0] row_mask:0xf bank_mask:0xf
	v_fmac_f32_dpp v53, v47, v50 quad_perm:[1,1,1,1] row_mask:0xf bank_mask:0xf
	v_fmac_f32_dpp v54, v47, v50 quad_perm:[2,2,2,2] row_mask:0xf bank_mask:0xf
	v_fmac_f32_dpp v52, v60, v51 quad_perm:[0,0,0,0] row_mask:0xf bank_mask:0xf
	v_fmac_f32_dpp v53, v60, v51 quad_perm:[1,1,1,1] row_mask:0xf bank_mask:0xf
	v_fmac_f32_dpp v54, v60, v51 quad_perm:[2,2,2,2] row_mask:0xf bank_mask:0xf
	v_mov_b32_e32 v55, 0
	v_writelane_b32 v55, s32, 48
	v_writelane_b32 v55, s33, 49
	v_writelane_b32 v55, s34, 50
	v_mul_f32_e32 v55, 0xbc800000, v55
	v_mul_f32_e32 v56, v55, v52
	v_mul_f32_e32 v57, v55, v53
	v_mul_f32_e32 v58, v55, v54
	v_add_f32_dpp v56, v56, v56 quad_perm:[1,0,3,2] row_mask:0xf bank_mask:0xf
	v_add_f32_dpp v57, v57, v57 quad_perm:[1,0,3,2] row_mask:0xf bank_mask:0xf
	v_add_f32_dpp v58, v58, v58 quad_perm:[1,0,3,2] row_mask:0xf bank_mask:0xf
	v_add_f32_dpp v56, v56, v56 quad_perm:[2,3,0,1] row_mask:0xf bank_mask:0xf
	v_add_f32_dpp v57, v57, v57 quad_perm:[2,3,0,1] row_mask:0xf bank_mask:0xf
	v_add_f32_dpp v58, v58, v58 quad_perm:[2,3,0,1] row_mask:0xf bank_mask:0xf
	v_cndmask_b32_e64 v52, v52, v56, s[26:27]
	v_cndmask_b32_e64 v53, v53, v57, s[26:27]
	v_cndmask_b32_e64 v54, v54, v58, s[26:27]
	v_subrev_u32_e32 v59, 48, v0
	v_lshlrev_b32_e32 v59, 4, v59
	s_mov_b32 s20, 0
	s_mov_b32 s21, 0xf0000
	s_mov_b64 exec, s[20:21]
	ds_write_b96 v59, v[52:54] offset:24576
	s_mov_b64 exec, -1
	s_waitcnt lgkmcnt(0)
	s_branch .Ljoin
.Lbulk_waves:
	global_load_dwordx4 v[8:11], v1, s[4:5] offset:-2048 sc1 nt
	global_load_dwordx4 v[12:15], v1, s[4:5] offset:-1024 sc1 nt
	global_load_dwordx4 v[16:19], v1, s[4:5] offset:0 sc1 nt
	global_load_dwordx4 v[20:23], v1, s[4:5] offset:1024 sc1 nt
	global_load_dwordx4 v[24:27], v1, s[4:5] offset:2048 sc1 nt
	s_and_saveexec_b64 s[16:17], s[14:15]
	global_load_dwordx4 v[28:31], v1, s[4:5] offset:3072 sc1 nt
	s_mov_b64 exec, s[16:17]
	s_waitcnt vmcnt(0)
	ds_write_b128 v2, v[8:11]
	ds_write_b128 v2, v[12:15] offset:1024
	ds_write_b128 v2, v[16:19] offset:2048
	ds_write_b128 v2, v[20:23] offset:3072
	ds_write_b128 v2, v[24:27] offset:4096
	ds_write_b128 v2, v[28:31] offset:5120
	s_waitcnt lgkmcnt(0)
	s_barrier
